# speedup vs baseline: 1.0038x; 1.0038x over previous
_Z9k_scatterPKiS0_PiPjPKfS4_S4_S4_PfS4_PDv4_j:
	s_load_dwordx4 s[4:7], s[0:1], 0x0
	s_mul_hi_i32 s9, s2, 0x30d4
	s_mul_i32 s8, s2, 0x30d4
	s_lshl_b64 s[24:25], s[8:9], 2
	v_or_b32_e32 v1, 0x400, v0
	s_waitcnt lgkmcnt(0)
	s_cmp_gt_u32 s2, 2
	s_cbranch_scc1 .Lk1_nopf
	s_load_dwordx8 s[36:43], s[0:1], 0x20
	s_load_dwordx2 s[44:45], s[0:1], 0x48
	v_cmp_gt_u32_e64 s[46:47], 64, v0
	s_and_saveexec_b64 s[48:49], s[46:47]
	v_lshlrev_b32_e32 v112, 6, v0
	s_waitcnt lgkmcnt(0)
	s_cmp_eq_u32 s2, 1
	s_cbranch_scc1 .Lk1_pfw1
	v_min_u32_e32 v108, 0x7c0, v112
	v_min_u32_e32 v109, 64, v112
	v_min_u32_e32 v110, 0xc0, v112
	v_mov_b32_e32 v111, 0
	global_load_dword v113, v108, s[36:37]
	global_load_dword v113, v109, s[38:39]
	global_load_dword v113, v110, s[40:41]
	global_load_dword v113, v111, s[42:43]
	s_branch .Lk1_pfend

.LBB0_18:
	s_or_b64 exec, exec, s[6:7]
	s_load_dwordx2 s[6:7], s[0:1], 0x18
	s_cmp_eq_u32 s2, 0
	v_add_u32_e32 v38, 0xfffffcc0, v0
	s_cselect_b64 s[8:9], -1, 0
	s_cmp_eq_u32 s2, 2
	s_cselect_b64 s[12:13], -1, 0
	v_cmp_gt_u32_e64 s[2:3], 32, v38
	v_add_u32_e32 v39, 0xffffffe0, v38
	v_cmp_gt_u32_e64 s[14:15], 2, v39
	s_and_b64 s[2:3], s[8:9], s[2:3]
	s_and_b64 s[14:15], s[12:13], s[14:15]
	s_or_b64 s[2:3], s[2:3], s[14:15]
	s_and_saveexec_b64 s[26:27], s[2:3]
	s_cbranch_execz .LBB0_26
	s_load_dwordx2 s[28:29], s[0:1], 0x40
	s_load_dwordx2 s[30:31], s[0:1], 0x30
	s_movk_i32 s2, 0x35f
	v_cmp_lt_u32_e64 s[2:3], s2, v0
	s_and_saveexec_b64 s[8:9], s[2:3]
	s_xor_b64 s[34:35], exec, s[8:9]
	s_cbranch_execz .LBB0_23
	v_add_u32_e32 v39, 0xfffffca0, v0
	v_lshlrev_b32_e32 v0, 5, v39
	v_mov_b32_e32 v1, 0
	s_waitcnt lgkmcnt(0)
	v_lshl_add_u64 v[0:1], v[0:1], 2, s[30:31]
	global_load_dwordx4 v[34:37], v[0:1], off
	global_load_dwordx4 v[40:43], v[0:1], off offset:80
	global_load_dwordx4 v[88:91], v[0:1], off offset:96
	global_load_dwordx4 v[92:95], v[0:1], off offset:112
	global_load_dwordx4 v[96:99], v[0:1], off offset:16
	global_load_dwordx4 v[100:103], v[0:1], off offset:32
	global_load_dwordx4 v[104:107], v[0:1], off offset:48
	global_load_dwordx4 v[108:111], v[0:1], off offset:64
	s_load_dwordx2 s[2:3], s[0:1], 0x28
	s_waitcnt lgkmcnt(0)
	s_load_dwordx16 s[36:51], s[2:3], 0x0
	s_load_dwordx16 s[8:23], s[2:3], 0x40
	v_cmp_eq_u32_e64 s[2:3], 0, v39
	s_waitcnt vmcnt(7) lgkmcnt(0)
	v_fma_f32 v34, s36, v34, 0
	v_fmac_f32_e32 v34, s37, v35
	v_fmac_f32_e32 v34, s38, v36
	v_fmac_f32_e32 v34, s39, v37
	s_waitcnt vmcnt(3)
	v_fmac_f32_e32 v34, s40, v96
	v_fmac_f32_e32 v34, s41, v97
	v_fmac_f32_e32 v34, s42, v98
	v_fmac_f32_e32 v34, s43, v99
	s_waitcnt vmcnt(2)
	v_fmac_f32_e32 v34, s44, v100
	v_fmac_f32_e32 v34, s45, v101
	v_fmac_f32_e32 v34, s46, v102
	v_fmac_f32_e32 v34, s47, v103
	s_waitcnt vmcnt(1)
	v_fmac_f32_e32 v34, s48, v104
	v_fmac_f32_e32 v34, s49, v105
	v_fmac_f32_e32 v34, s50, v106
	v_fmac_f32_e32 v34, s51, v107
	s_waitcnt vmcnt(0)
	v_fmac_f32_e32 v34, s8, v108
	v_fmac_f32_e32 v34, s9, v109
	v_fmac_f32_e32 v34, s10, v110
	v_pk_mul_f32 v[0:1], s[12:13], v[40:41]
	v_fmac_f32_e32 v34, s11, v111
	v_add_f32_e32 v0, v34, v0
	v_pk_mul_f32 v[40:41], s[14:15], v[42:43]
	v_add_f32_e32 v0, v0, v1
	v_add_f32_e32 v0, v0, v40
	v_pk_mul_f32 v[42:43], s[16:17], v[88:89]
	v_add_f32_e32 v0, v0, v41
	v_add_f32_e32 v0, v0, v42
	v_pk_mul_f32 v[88:89], s[18:19], v[90:91]
	v_add_f32_e32 v0, v0, v43
	v_add_f32_e32 v0, v0, v88
	v_pk_mul_f32 v[90:91], s[20:21], v[92:93]
	v_add_f32_e32 v0, v0, v89
	v_add_f32_e32 v0, v0, v90
	v_pk_mul_f32 v[92:93], s[22:23], v[94:95]
	v_add_f32_e32 v0, v0, v91
	v_add_f32_e32 v0, v0, v92
	v_add_f32_e32 v1, v0, v93
	s_and_saveexec_b64 s[8:9], s[2:3]
	s_cbranch_execz .LBB0_22
	s_load_dwordx2 s[2:3], s[0:1], 0x38
	s_waitcnt lgkmcnt(0)
	s_load_dword s2, s[2:3], 0x0
	s_waitcnt lgkmcnt(0)
	v_add_f32_e32 v1, s2, v1
